# ret_kv (p3): logsigmoid(gamma) lane table once per phase instead of twice per item
# baseline (speedup 1.0000x reference)
.LBB0_984:
	s_andn2_b64 vcc, exec, s[10:11]
	s_cbranch_vccnz .LBB0_998
	s_lshl_b32 s10, s8, 4
	s_ashr_i32 s11, s10, 31
	v_readlane_b32 s16, v233, 0
	s_ashr_i32 s9, s12, 8
	s_lshl_b64 s[10:11], s[10:11], 2
	v_readlane_b32 s26, v233, 10
	v_readlane_b32 s27, v233, 11
	s_add_u32 s10, s26, s10
	s_addc_u32 s11, s27, s11
	v_readlane_b32 s17, v233, 1
	s_add_u32 s16, s6, 0x27400000
	s_addc_u32 s17, s7, 0
	s_lshl_b32 s62, s96, 1
	s_add_i32 s13, s9, s62
	s_ashr_i32 s14, s13, 31
	v_readlane_b32 s18, v233, 2
	s_bfe_u32 s3, s12, 0x20006
	s_lshr_b32 s12, s14, 27
	s_add_i32 s18, s13, s12
	s_and_b32 s12, s18, 0xffffffe0
	s_lshr_b32 s14, s14, 24
	s_sub_i32 s12, s13, s12
	s_add_i32 s13, s13, s14
	s_ashr_i32 s14, s13, 8
	s_mul_i32 s2, s9, 0xd800
	s_ashr_i32 s15, s14, 31
	s_ashr_i32 s13, s12, 31
	s_add_i32 s2, s2, 0
	s_lshl_b64 s[14:15], s[14:15], 12
	s_lshl_b64 s[12:13], s[12:13], 7
	s_add_u32 s12, s14, s12
	s_addc_u32 s13, s15, s13
	s_mulk_i32 s13, 0x3400
	s_mul_hi_u32 s14, s12, 0x3400
	s_add_i32 s14, s14, s13
	s_mulk_i32 s12, 0x3400
	s_add_u32 s12, s0, s12
	s_addc_u32 s13, s1, s14
	s_lshl_b32 s14, s18, 2
	s_and_b32 s14, s14, 0x380
	v_bfe_u32 v37, v1, 3, 5
	s_add_u32 s12, s12, s14
	v_mul_u32_u24_e32 v36, 0x1a00, v37
	s_addc_u32 s13, s13, 0
	v_and_b32_e32 v38, 56, v144
	v_mov_b32_e32 v35, 0
	v_lshlrev_b32_e32 v34, 1, v36
	v_lshl_add_u64 v[2:3], s[12:13], 0, v[34:35]
	v_lshlrev_b32_e32 v34, 1, v38
	v_lshl_add_u64 v[26:27], v[2:3], 0, v[34:35]
	s_mov_b32 s12, 0x68000
	v_add_co_u32_e32 v14, vcc, s12, v26
	s_mov_b32 s12, 0xd0000
	s_nop 0
	v_addc_co_u32_e32 v15, vcc, 0, v27, vcc
	v_add_co_u32_e32 v22, vcc, s12, v26
	s_mov_b32 s12, 0x138000
	s_nop 0
	v_addc_co_u32_e32 v23, vcc, 0, v27, vcc
	v_add_co_u32_e32 v30, vcc, s12, v26
	global_load_dwordx4 v[2:5], v[26:27], off offset:1024
	global_load_dwordx4 v[6:9], v[26:27], off offset:2048
	v_addc_co_u32_e32 v31, vcc, 0, v27, vcc
	global_load_dwordx4 v[10:13], v[14:15], off offset:1024
	s_nop 0
	global_load_dwordx4 v[14:17], v[14:15], off offset:2048
	s_nop 0
	global_load_dwordx4 v[18:21], v[22:23], off offset:1024
	s_nop 0
	global_load_dwordx4 v[22:25], v[22:23], off offset:2048
	s_nop 0
	global_load_dwordx4 v[26:29], v[30:31], off offset:1024
	s_nop 0
	global_load_dwordx4 v[30:33], v[30:31], off offset:2048
	v_lshlrev_b32_e32 v43, 6, v146
	v_lshrrev_b32_e32 v40, 3, v1
	s_lshl_b32 s12, s3, 5
	v_lshl_or_b32 v44, s3, 10, v43
	s_movk_i32 s3, 0x7f
	v_bitop3_b32 v43, v40, s3, 31 bitop3:0x6c
	v_cvt_f32_ubyte0_e32 v46, v43
	v_mul_u32_u24_e32 v43, 0x48, v37
	v_lshlrev_b32_e32 v43, 1, v43
	s_movk_i32 s3, 0x5f
	v_add3_u32 v48, s2, v34, v43
	v_bitop3_b32 v43, v40, s3, 31 bitop3:0x6c
	v_lshl_or_b32 v39, v145, 3, v39
	v_cvt_f32_ubyte0_e32 v47, v37
	v_or_b32_e32 v34, 32, v37
	v_cvt_f32_ubyte0_e32 v49, v43
	v_or_b32_e32 v43, 64, v37
	v_or_b32_e32 v37, 0x60, v37
	v_cvt_f32_ubyte0_e32 v54, v37
	v_mul_u32_u24_e32 v37, 0x48, v39
	v_readlane_b32 s19, v233, 3
	v_readlane_b32 s20, v233, 4
	v_readlane_b32 s21, v233, 5
	v_readlane_b32 s22, v233, 6
	v_readlane_b32 s23, v233, 7
	v_readlane_b32 s24, v233, 8
	v_readlane_b32 s25, v233, 9
	v_readlane_b32 s28, v233, 12
	v_readlane_b32 s29, v233, 13
	s_lshl_b32 s18, s90, 1
	s_add_i32 s12, s2, s12
	v_and_b32_e32 v41, 24, v144
	v_lshlrev_b32_e32 v42, 2, v145
	v_cvt_f32_ubyte0_e32 v50, v34
	v_bitop3_b32 v45, v40, 63, 31 bitop3:0x6c
	v_bitop3_b32 v40, v40, 31, v40 bitop3:0xc
	v_mul_u32_u24_e32 v34, 0x1a00, v34
	v_lshlrev_b32_e32 v37, 1, v37
	v_cvt_f32_ubyte0_e32 v51, v45
	v_cvt_f32_ubyte0_e32 v52, v43
	v_cvt_f32_ubyte0_e32 v53, v40
	v_add3_u32 v55, s12, v41, v37
	v_add3_u32 v56, s2, v41, v37
	s_add_i32 s19, s9, s18
	s_mov_b32 s20, 0xbfb8aa3b
	s_mov_b32 s21, 0x42ce8ed0
	s_mov_b32 s22, 0xc2b17218
	s_mov_b32 s23, 0x7f800000
	s_mov_b32 s24, 0x3f2aaaab
	v_mov_b32_e32 v57, 0x3ecc95a3
	s_mov_b32 s25, 0x3f317218
	s_mov_b32 s26, 0x33800000
	s_mov_b32 s27, 0x3fb8aa3b
	s_mov_b32 s28, 0xc2ce8ed0
	s_mov_b32 s29, 0x42b17218
	v_lshlrev_b32_e32 v36, 1, v36
	v_lshlrev_b32_e32 v38, 1, v38
	v_lshlrev_b32_e32 v40, 1, v34
	v_lshlrev_b32_e32 v34, 1, v44
	v_lshlrev_b32_e32 v42, 1, v42
	v_mov_b32_e32 v58, 0x7f800000
	v_mov_b32_e32 v44, 0x3f317218
	s_mov_b32 s36, s62
	v_readlane_b32 s30, v233, 14
	v_readlane_b32 s31, v233, 15
	v_mbcnt_lo_u32_b32 v231, -1, 0
	v_mbcnt_hi_u32_b32 v231, -1, v231
	s_mov_b32 s30, 0
.Llsg_rk0_loop:
	s_lshl_b32 s2, s30, 2
	v_mov_b32_e32 v37, s2
	global_load_dword v39, v37, s[10:11]
	s_waitcnt vmcnt(0)
	v_cmp_ngt_f32_e32 vcc, 0, v39
	s_cbranch_vccz .Llsg_rk0_a
	v_mul_f32_e32 v37, 0xbfb8aa3b, v39
	v_rndne_f32_e32 v41, v37
	v_sub_f32_e32 v43, v37, v41
	v_fma_f32 v37, v39, s20, -v37
	v_fmac_f32_e32 v37, 0xb2a5705f, v39
	v_add_f32_e32 v37, v43, v37
	v_cvt_i32_f32_e32 v41, v41
	v_exp_f32_e32 v37, v37
	v_cmp_nlt_f32_e32 vcc, s21, v39
	v_ldexp_f32 v37, v37, v41
	s_nop 0
	v_cndmask_b32_e32 v37, 0, v37, vcc
	v_cmp_ngt_f32_e32 vcc, s22, v39
	s_nop 1
	v_cndmask_b32_e32 v37, v58, v37, vcc
	v_add_f32_e32 v41, 1.0, v37
	v_add_f32_e32 v43, -1.0, v41
	v_sub_f32_e32 v45, v43, v41
	v_add_f32_e32 v45, 1.0, v45
	v_sub_f32_e32 v43, v37, v43
	v_add_f32_e32 v43, v43, v45
	v_frexp_mant_f32_e32 v45, v41
	v_cvt_f64_f32_e32 v[60:61], v41
	v_frexp_exp_i32_f64_e32 v59, v[60:61]
	v_cmp_gt_f32_e32 vcc, s24, v45
	s_nop 1
	v_subbrev_co_u32_e32 v59, vcc, 0, v59, vcc
	v_sub_u32_e32 v45, 0, v59
	v_ldexp_f32 v41, v41, v45
	v_ldexp_f32 v43, v43, v45
	v_add_f32_e32 v45, -1.0, v41
	v_add_f32_e32 v61, 1.0, v41
	v_add_f32_e32 v60, 1.0, v45
	v_add_f32_e32 v62, -1.0, v61
	v_sub_f32_e32 v60, v41, v60
	v_sub_f32_e32 v41, v41, v62
	v_add_f32_e32 v41, v43, v41
	v_add_f32_e32 v60, v43, v60
	v_add_f32_e32 v43, v61, v41
	v_rcp_f32_e32 v68, v43
	v_sub_f32_e32 v61, v61, v43
	v_add_f32_e32 v41, v41, v61
	v_add_f32_e32 v61, v45, v60
	v_mul_f32_e32 v69, v61, v68
	v_mul_f32_e32 v62, v43, v69
	v_fma_f32 v64, v69, v43, -v62
	v_sub_f32_e32 v45, v45, v61
	v_fmac_f32_e32 v64, v69, v41
	v_add_f32_e32 v45, v60, v45
	v_add_f32_e32 v60, v62, v64
	v_sub_f32_e32 v63, v61, v60
	v_pk_add_f32 v[66:67], v[60:61], v[62:63] neg_lo:[0,1] neg_hi:[0,1]
	v_mov_b32_e32 v65, v60
	v_pk_add_f32 v[60:61], v[66:67], v[64:65] neg_lo:[0,1] neg_hi:[0,1]
	v_cmp_neq_f32_e32 vcc, s23, v37
	v_add_f32_e32 v45, v45, v61
	v_add_f32_e32 v45, v60, v45
	v_add_f32_e32 v61, v63, v45
	v_mul_f32_e32 v70, v68, v61
	v_mul_f32_e32 v62, v43, v70
	v_fma_f32 v64, v70, v43, -v62
	v_fmac_f32_e32 v64, v70, v41
	v_add_f32_e32 v60, v62, v64
	v_sub_f32_e32 v41, v63, v61
	v_sub_f32_e32 v63, v61, v60
	v_pk_add_f32 v[66:67], v[60:61], v[62:63] neg_lo:[0,1] neg_hi:[0,1]
	v_mov_b32_e32 v65, v60
	v_add_f32_e32 v41, v45, v41
	v_pk_add_f32 v[60:61], v[66:67], v[64:65] neg_lo:[0,1] neg_hi:[0,1]
	v_add_f32_e32 v43, v69, v70
	v_add_f32_e32 v41, v41, v61
	v_add_f32_e32 v41, v60, v41
	v_add_f32_e32 v41, v63, v41
	v_sub_f32_e32 v45, v43, v69
	v_mul_f32_e32 v41, v68, v41
	v_sub_f32_e32 v45, v70, v45
	v_add_f32_e32 v41, v45, v41
	v_add_f32_e32 v61, v43, v41
	v_cvt_f32_i32_e32 v60, v59
	v_mul_f32_e32 v62, v61, v61
	v_fmamk_f32 v45, v62, 0x3e9b6dac, v57
	v_fmaak_f32 v45, v62, v45, 0x3f2aaada
	v_sub_f32_e32 v43, v61, v43
	v_ldexp_f32 v63, v61, 1
	v_mul_f32_e32 v61, v61, v62
	v_pk_mul_f32 v[64:65], v[60:61], v[44:45]
	v_sub_f32_e32 v41, v41, v43
	v_fma_f32 v62, v60, s25, -v64
	v_fmac_f32_e32 v62, 0xb102e308, v60
	v_pk_add_f32 v[60:61], v[64:65], v[62:63]
	v_ldexp_f32 v41, v41, 1
	v_sub_f32_e32 v43, v61, v63
	v_sub_f32_e32 v43, v65, v43
	v_add_f32_e32 v67, v41, v43
	v_mov_b32_e32 v66, v64
	v_pk_add_f32 v[64:65], v[60:61], v[64:65] neg_lo:[0,1] neg_hi:[0,1]
	v_pk_add_f32 v[68:69], v[60:61], v[66:67]
	v_mov_b32_e32 v63, v60
	v_mov_b32_e32 v65, v69
	v_pk_add_f32 v[70:71], v[62:63], v[64:65] neg_lo:[0,1] neg_hi:[0,1]
	v_pk_add_f32 v[62:63], v[62:63], v[64:65]
	v_mov_b32_e32 v74, v61
	v_pk_add_f32 v[64:65], v[62:63], v[60:61] op_sel:[1,0] op_sel_hi:[0,1] neg_lo:[0,1] neg_hi:[0,1]
	v_pk_add_f32 v[72:73], v[68:69], v[64:65] op_sel_hi:[1,0] neg_lo:[0,1] neg_hi:[0,1]
	v_mov_b32_e32 v68, v69
	v_mov_b32_e32 v69, v63
	v_mov_b32_e32 v75, v64
	v_pk_add_f32 v[64:65], v[68:69], v[74:75] neg_lo:[0,1] neg_hi:[0,1]
	v_mov_b32_e32 v66, v67
	v_mov_b32_e32 v67, v60
	v_pk_add_f32 v[60:61], v[66:67], v[64:65] neg_lo:[0,1] neg_hi:[0,1]
	v_mov_b32_e32 v72, v70
	v_pk_add_f32 v[64:65], v[72:73], v[60:61]
	v_mov_b32_e32 v71, v63
	v_pk_add_f32 v[66:67], v[64:65], v[64:65] op_sel:[0,1] op_sel_hi:[1,0]
	s_nop 0
	v_pk_add_f32 v[62:63], v[62:63], v[66:67] op_sel:[1,0] op_sel_hi:[0,1]
	v_mov_b32_e32 v65, v62
	v_pk_add_f32 v[68:69], v[64:65], v[70:71] neg_lo:[0,1] neg_hi:[0,1]
	v_mov_b32_e32 v61, v66
	v_sub_f32_e32 v41, v64, v68
	v_pk_add_f32 v[60:61], v[60:61], v[68:69] neg_lo:[0,1] neg_hi:[0,1]
	v_sub_f32_e32 v41, v70, v41
	v_add_f32_e32 v41, v60, v41
	v_add_f32_e32 v41, v41, v61
	v_add_f32_e32 v41, v62, v41
	v_cndmask_b32_e32 v41, v58, v41, vcc
	v_cmp_lt_f32_e64 vcc, |v37|, s26
	s_nop 1
	v_cndmask_b32_e32 v37, v41, v37, vcc
	v_xor_b32_e32 v37, 0x80000000, v37
	s_cbranch_execz .Llsg_rk0_b
	s_branch .Llsg_rk0_c

.Llsg_rk0_c:
	s_nop 0
	v_cmp_eq_u32_e32 vcc, s30, v231
	s_nop 1
	v_cndmask_b32_e32 v230, v230, v37, vcc
	s_add_i32 s30, s30, 1
	s_cmp_lt_u32 s30, 16
	s_cbranch_scc1 .Llsg_rk0_loop
	s_branch .LBB0_987

.LBB0_987:
	s_add_i32 s31, s9, s36
	s_ashr_i32 s34, s31, 31
	s_lshr_b32 s2, s34, 27
	s_add_i32 s2, s31, s2
	s_ashr_i32 s35, s2, 5
	s_and_b32 s30, s35, 7
	s_lshl_b32 s2, s30, 2
	v_mov_b32_e32 v37, s2
	s_add_u32 s12, s10, s2
	s_addc_u32 s13, s11, 0
	s_waitcnt vmcnt(0)
	v_readlane_b32 vcc_lo, v230, s30
	s_add_i32 vcc_hi, s30, 8
	s_nop 1
	v_mov_b32_e32 v37, vcc_lo
	v_readlane_b32 vcc_lo, v230, vcc_hi
	s_nop 1
	v_mov_b32_e32 v41, vcc_lo

.LBB0_3302:
	s_andn2_b64 vcc, exec, s[12:13]
	s_cbranch_vccnz .LBB0_3316
	v_readlane_b32 s12, v233, 0
	s_lshl_b32 s2, s6, 4
	v_readlane_b32 s16, v233, 4
	v_readlane_b32 s17, v233, 5
	v_readlane_b32 s18, v233, 6
	v_readlane_b32 s19, v233, 7
	v_readlane_b32 s20, v233, 8
	v_readlane_b32 s21, v233, 9
	s_ashr_i32 s3, s2, 31
	v_readlane_b32 s22, v233, 10
	v_readlane_b32 s23, v233, 11
	v_readlane_b32 s24, v233, 12
	v_readlane_b32 s25, v233, 13
	s_mov_b64 s[16:17], s[20:21]
	s_ashr_i32 s7, s10, 8
	s_lshl_b64 s[2:3], s[2:3], 2
	s_mov_b64 s[18:19], s[22:23]
	v_readlane_b32 s13, v233, 1
	s_add_u32 s12, s18, s2
	s_addc_u32 s13, s19, s3
	s_add_u32 s8, s4, 0x27400000
	s_addc_u32 s9, s5, 0
	s_lshl_b32 s60, s96, 1
	v_readlane_b32 s15, v233, 3
	s_add_i32 s3, s7, s60
	v_readlane_b32 s14, v233, 2
	s_mul_i32 s2, s7, 0xd800
	s_bfe_u32 s15, s10, 0x20006
	s_ashr_i32 s10, s3, 31
	s_add_i32 s14, s2, 0
	s_lshr_b32 s2, s10, 27
	s_add_i32 s16, s3, s2
	s_and_b32 s2, s16, 0xffffffe0
	s_lshr_b32 s10, s10, 24
	s_sub_i32 s2, s3, s2
	s_add_i32 s3, s3, s10
	s_ashr_i32 s10, s3, 8
	s_ashr_i32 s11, s10, 31
	s_ashr_i32 s3, s2, 31
	s_lshl_b64 s[10:11], s[10:11], 12
	s_lshl_b64 s[2:3], s[2:3], 7
	s_add_u32 s2, s10, s2
	s_addc_u32 s3, s11, s3
	s_mulk_i32 s3, 0x3400
	s_mul_hi_u32 s10, s2, 0x3400
	s_add_i32 s10, s10, s3
	s_mulk_i32 s2, 0x3400
	s_add_u32 s2, s0, s2
	s_addc_u32 s3, s1, s10
	s_lshl_b32 s10, s16, 2
	s_and_b32 s10, s10, 0x380
	s_waitcnt vmcnt(0)
	v_bfe_u32 v37, v1, 3, 5
	s_add_u32 s2, s2, s10
	v_mul_u32_u24_e32 v36, 0x1a00, v37
	s_addc_u32 s3, s3, 0
	v_and_b32_e32 v38, 56, v119
	v_mov_b32_e32 v35, 0
	v_lshlrev_b32_e32 v34, 1, v36
	v_lshl_add_u64 v[2:3], s[2:3], 0, v[34:35]
	v_lshlrev_b32_e32 v34, 1, v38
	v_lshl_add_u64 v[26:27], v[2:3], 0, v[34:35]
	s_mov_b32 s2, 0x68000
	v_add_co_u32_e32 v14, vcc, s2, v26
	s_mov_b32 s2, 0xd0000
	s_nop 0
	v_addc_co_u32_e32 v15, vcc, 0, v27, vcc
	v_add_co_u32_e32 v22, vcc, s2, v26
	s_mov_b32 s2, 0x138000
	s_nop 0
	v_addc_co_u32_e32 v23, vcc, 0, v27, vcc
	v_add_co_u32_e32 v30, vcc, s2, v26
	global_load_dwordx4 v[2:5], v[26:27], off offset:1024
	global_load_dwordx4 v[6:9], v[26:27], off offset:2048
	v_addc_co_u32_e32 v31, vcc, 0, v27, vcc
	global_load_dwordx4 v[10:13], v[14:15], off offset:1024
	s_nop 0
	global_load_dwordx4 v[14:17], v[14:15], off offset:2048
	s_nop 0
	global_load_dwordx4 v[18:21], v[22:23], off offset:1024
	s_nop 0
	global_load_dwordx4 v[22:25], v[22:23], off offset:2048
	s_nop 0
	global_load_dwordx4 v[26:29], v[30:31], off offset:1024
	s_nop 0
	global_load_dwordx4 v[30:33], v[30:31], off offset:2048
	v_lshrrev_b32_e32 v39, 3, v1
	v_lshlrev_b32_e32 v43, 6, v111
	s_movk_i32 s3, 0x7f
	v_lshl_or_b32 v44, s15, 10, v43
	v_bitop3_b32 v43, v39, s3, 31 bitop3:0x6c
	v_cvt_f32_ubyte0_e32 v46, v43
	v_mul_u32_u24_e32 v43, 0x48, v37
	v_lshlrev_b32_e32 v43, 1, v43
	s_movk_i32 s3, 0x5f
	v_add3_u32 v48, s14, v34, v43
	v_bitop3_b32 v43, v39, s3, 31 bitop3:0x6c
	v_lshl_or_b32 v40, v110, 3, v112
	v_cvt_f32_ubyte0_e32 v47, v37
	v_or_b32_e32 v34, 32, v37
	v_cvt_f32_ubyte0_e32 v49, v43
	v_or_b32_e32 v43, 64, v37
	v_or_b32_e32 v37, 0x60, v37
	s_lshl_b32 s2, s15, 5
	v_cvt_f32_ubyte0_e32 v54, v37
	v_mul_u32_u24_e32 v37, 0x48, v40
	v_readlane_b32 s26, v233, 14
	v_readlane_b32 s27, v233, 15
	s_mov_b64 s[20:21], s[24:25]
	s_lshl_b32 s10, s76, 1
	s_add_i32 s2, s14, s2
	v_and_b32_e32 v41, 24, v119
	v_lshlrev_b32_e32 v42, 2, v110
	v_cvt_f32_ubyte0_e32 v50, v34
	v_bitop3_b32 v45, v39, 63, 31 bitop3:0x6c
	v_bitop3_b32 v39, v39, 31, v39 bitop3:0xc
	v_mul_u32_u24_e32 v34, 0x1a00, v34
	v_lshlrev_b32_e32 v37, 1, v37
	v_cvt_f32_ubyte0_e32 v51, v45
	v_cvt_f32_ubyte0_e32 v52, v43
	v_cvt_f32_ubyte0_e32 v53, v39
	v_add3_u32 v55, s2, v41, v37
	v_add3_u32 v56, s14, v41, v37
	s_add_i32 s11, s7, s10
	s_mov_b32 s18, 0xbfb8aa3b
	s_mov_b32 s19, 0x42ce8ed0
	s_mov_b32 s20, 0xc2b17218
	s_mov_b32 s21, 0x7f800000
	s_mov_b32 s22, 0x3f2aaaab
	v_mov_b32_e32 v57, 0x3ecc95a3
	s_mov_b32 s23, 0x3f317218
	s_mov_b32 s24, 0x33800000
	s_mov_b32 s25, 0x3fb8aa3b
	s_mov_b32 s26, 0xc2ce8ed0
	s_mov_b32 s27, 0x42b17218
	v_lshlrev_b32_e32 v36, 1, v36
	v_lshlrev_b32_e32 v38, 1, v38
	v_lshlrev_b32_e32 v40, 1, v34
	v_lshlrev_b32_e32 v34, 1, v44
	v_lshlrev_b32_e32 v42, 1, v42
	v_mov_b32_e32 v58, 0x7f800000
	v_mov_b32_e32 v44, 0x3f317218
	s_mov_b32 s34, s60
	v_mbcnt_lo_u32_b32 v231, -1, 0
	v_mbcnt_hi_u32_b32 v231, -1, v231
	s_mov_b32 s28, 0
.Llsg_rk1_loop:
	s_lshl_b32 s2, s28, 2
	v_mov_b32_e32 v37, s2
	global_load_dword v39, v37, s[12:13]
	s_waitcnt vmcnt(0)
	v_cmp_ngt_f32_e32 vcc, 0, v39
	s_cbranch_vccz .Llsg_rk1_a
	v_mul_f32_e32 v37, 0xbfb8aa3b, v39
	v_rndne_f32_e32 v41, v37
	v_sub_f32_e32 v43, v37, v41
	v_fma_f32 v37, v39, s18, -v37
	v_fmac_f32_e32 v37, 0xb2a5705f, v39
	v_add_f32_e32 v37, v43, v37
	v_cvt_i32_f32_e32 v41, v41
	v_exp_f32_e32 v37, v37
	v_cmp_nlt_f32_e32 vcc, s19, v39
	v_ldexp_f32 v37, v37, v41
	s_nop 0
	v_cndmask_b32_e32 v37, 0, v37, vcc
	v_cmp_ngt_f32_e32 vcc, s20, v39
	s_nop 1
	v_cndmask_b32_e32 v37, v58, v37, vcc
	v_add_f32_e32 v41, 1.0, v37
	v_add_f32_e32 v43, -1.0, v41
	v_sub_f32_e32 v45, v43, v41
	v_add_f32_e32 v45, 1.0, v45
	v_sub_f32_e32 v43, v37, v43
	v_add_f32_e32 v43, v43, v45
	v_frexp_mant_f32_e32 v45, v41
	v_cvt_f64_f32_e32 v[60:61], v41
	v_frexp_exp_i32_f64_e32 v59, v[60:61]
	v_cmp_gt_f32_e32 vcc, s22, v45
	s_nop 1
	v_subbrev_co_u32_e32 v59, vcc, 0, v59, vcc
	v_sub_u32_e32 v45, 0, v59
	v_ldexp_f32 v41, v41, v45
	v_ldexp_f32 v43, v43, v45
	v_add_f32_e32 v45, -1.0, v41
	v_add_f32_e32 v61, 1.0, v41
	v_add_f32_e32 v60, 1.0, v45
	v_add_f32_e32 v62, -1.0, v61
	v_sub_f32_e32 v60, v41, v60
	v_sub_f32_e32 v41, v41, v62
	v_add_f32_e32 v41, v43, v41
	v_add_f32_e32 v60, v43, v60
	v_add_f32_e32 v43, v61, v41
	v_rcp_f32_e32 v68, v43
	v_sub_f32_e32 v61, v61, v43
	v_add_f32_e32 v41, v41, v61
	v_add_f32_e32 v61, v45, v60
	v_mul_f32_e32 v69, v61, v68
	v_mul_f32_e32 v62, v43, v69
	v_fma_f32 v64, v69, v43, -v62
	v_sub_f32_e32 v45, v45, v61
	v_fmac_f32_e32 v64, v69, v41
	v_add_f32_e32 v45, v60, v45
	v_add_f32_e32 v60, v62, v64
	v_sub_f32_e32 v63, v61, v60
	v_pk_add_f32 v[66:67], v[60:61], v[62:63] neg_lo:[0,1] neg_hi:[0,1]
	v_mov_b32_e32 v65, v60
	v_pk_add_f32 v[60:61], v[66:67], v[64:65] neg_lo:[0,1] neg_hi:[0,1]
	v_cmp_neq_f32_e32 vcc, s21, v37
	v_add_f32_e32 v45, v45, v61
	v_add_f32_e32 v45, v60, v45
	v_add_f32_e32 v61, v63, v45
	v_mul_f32_e32 v70, v68, v61
	v_mul_f32_e32 v62, v43, v70
	v_fma_f32 v64, v70, v43, -v62
	v_fmac_f32_e32 v64, v70, v41
	v_add_f32_e32 v60, v62, v64
	v_sub_f32_e32 v41, v63, v61
	v_sub_f32_e32 v63, v61, v60
	v_pk_add_f32 v[66:67], v[60:61], v[62:63] neg_lo:[0,1] neg_hi:[0,1]
	v_mov_b32_e32 v65, v60
	v_add_f32_e32 v41, v45, v41
	v_pk_add_f32 v[60:61], v[66:67], v[64:65] neg_lo:[0,1] neg_hi:[0,1]
	v_add_f32_e32 v43, v69, v70
	v_add_f32_e32 v41, v41, v61
	v_add_f32_e32 v41, v60, v41
	v_add_f32_e32 v41, v63, v41
	v_sub_f32_e32 v45, v43, v69
	v_mul_f32_e32 v41, v68, v41
	v_sub_f32_e32 v45, v70, v45
	v_add_f32_e32 v41, v45, v41
	v_add_f32_e32 v61, v43, v41
	v_cvt_f32_i32_e32 v60, v59
	v_mul_f32_e32 v62, v61, v61
	v_fmamk_f32 v45, v62, 0x3e9b6dac, v57
	v_fmaak_f32 v45, v62, v45, 0x3f2aaada
	v_sub_f32_e32 v43, v61, v43
	v_ldexp_f32 v63, v61, 1
	v_mul_f32_e32 v61, v61, v62
	v_pk_mul_f32 v[64:65], v[60:61], v[44:45]
	v_sub_f32_e32 v41, v41, v43
	v_fma_f32 v62, v60, s23, -v64
	v_fmac_f32_e32 v62, 0xb102e308, v60
	v_pk_add_f32 v[60:61], v[64:65], v[62:63]
	v_ldexp_f32 v41, v41, 1
	v_sub_f32_e32 v43, v61, v63
	v_sub_f32_e32 v43, v65, v43
	v_add_f32_e32 v67, v41, v43
	v_mov_b32_e32 v66, v64
	v_pk_add_f32 v[64:65], v[60:61], v[64:65] neg_lo:[0,1] neg_hi:[0,1]
	v_pk_add_f32 v[68:69], v[60:61], v[66:67]
	v_mov_b32_e32 v63, v60
	v_mov_b32_e32 v65, v69
	v_pk_add_f32 v[70:71], v[62:63], v[64:65] neg_lo:[0,1] neg_hi:[0,1]
	v_pk_add_f32 v[62:63], v[62:63], v[64:65]
	v_mov_b32_e32 v74, v61
	v_pk_add_f32 v[64:65], v[62:63], v[60:61] op_sel:[1,0] op_sel_hi:[0,1] neg_lo:[0,1] neg_hi:[0,1]
	v_pk_add_f32 v[72:73], v[68:69], v[64:65] op_sel_hi:[1,0] neg_lo:[0,1] neg_hi:[0,1]
	v_mov_b32_e32 v68, v69
	v_mov_b32_e32 v69, v63
	v_mov_b32_e32 v75, v64
	v_pk_add_f32 v[64:65], v[68:69], v[74:75] neg_lo:[0,1] neg_hi:[0,1]
	v_mov_b32_e32 v66, v67
	v_mov_b32_e32 v67, v60
	v_pk_add_f32 v[60:61], v[66:67], v[64:65] neg_lo:[0,1] neg_hi:[0,1]
	v_mov_b32_e32 v72, v70
	v_pk_add_f32 v[64:65], v[72:73], v[60:61]
	v_mov_b32_e32 v71, v63
	v_pk_add_f32 v[66:67], v[64:65], v[64:65] op_sel:[0,1] op_sel_hi:[1,0]
	s_nop 0
	v_pk_add_f32 v[62:63], v[62:63], v[66:67] op_sel:[1,0] op_sel_hi:[0,1]
	v_mov_b32_e32 v65, v62
	v_pk_add_f32 v[68:69], v[64:65], v[70:71] neg_lo:[0,1] neg_hi:[0,1]
	v_mov_b32_e32 v61, v66
	v_sub_f32_e32 v41, v64, v68
	v_pk_add_f32 v[60:61], v[60:61], v[68:69] neg_lo:[0,1] neg_hi:[0,1]
	v_sub_f32_e32 v41, v70, v41
	v_add_f32_e32 v41, v60, v41
	v_add_f32_e32 v41, v41, v61
	v_add_f32_e32 v41, v62, v41
	v_cndmask_b32_e32 v41, v58, v41, vcc
	v_cmp_lt_f32_e64 vcc, |v37|, s24
	s_nop 1
	v_cndmask_b32_e32 v37, v41, v37, vcc
	v_xor_b32_e32 v37, 0x80000000, v37
	s_cbranch_execz .Llsg_rk1_b
	s_branch .Llsg_rk1_c

.Llsg_rk1_c:
	s_nop 0
	v_cmp_eq_u32_e32 vcc, s28, v231
	s_nop 1
	v_cndmask_b32_e32 v230, v230, v37, vcc
	s_add_i32 s28, s28, 1
	s_cmp_lt_u32 s28, 16
	s_cbranch_scc1 .Llsg_rk1_loop
	s_branch .LBB0_3305

.LBB0_3305:
	s_add_i32 s29, s7, s34
	s_ashr_i32 s30, s29, 31
	s_lshr_b32 s2, s30, 27
	s_add_i32 s2, s29, s2
	s_ashr_i32 s31, s2, 5
	s_and_b32 s28, s31, 7
	s_lshl_b32 s2, s28, 2
	v_mov_b32_e32 v37, s2
	s_add_u32 s14, s12, s2
	s_addc_u32 s15, s13, 0
	s_waitcnt vmcnt(0)
	v_readlane_b32 vcc_lo, v230, s28
	s_add_i32 vcc_hi, s28, 8
	s_nop 1
	v_mov_b32_e32 v37, vcc_lo
	v_readlane_b32 vcc_lo, v230, vcc_hi
	s_nop 1
	v_mov_b32_e32 v41, vcc_lo
